# speedup vs baseline: 1.0085x; 1.0085x over previous
_Z11attn_kernelPKDF16_S0_PDF16_:
	s_load_dwordx4 s[4:7], s[0:1], 0x0
	s_load_dwordx2 s[8:9], s[0:1], 0x10
	s_lshr_b32 s1, s2, 3
	s_lshr_b32 s10, s2, 7
	s_and_b32 s0, s2, 4
	s_and_b32 s1, s1, 8
	s_and_b32 s20, s2, 3
	s_lshl_b32 s30, s10, 4
	s_or_b32 s22, s1, s0
	s_or_b32 s0, s30, s20
	s_or_b32 s14, s0, s22
	s_or_b32 s0, s20, 16
	s_sub_i32 s0, s0, s30
	s_mov_b32 s15, 0
	s_or_b32 s0, s0, s22
	s_bfe_u32 s24, s2, 0x30003
	s_ashr_i32 s1, s0, 31
	s_lshl_b64 s[2:3], s[14:15], 18
	s_waitcnt lgkmcnt(0)
	s_add_u32 s2, s4, s2
	s_addc_u32 s3, s5, s3
	s_lshl_b64 s[0:1], s[0:1], 18
	s_add_u32 s11, s4, s0
	s_addc_u32 s12, s5, s1
	s_add_u32 s13, s6, s0
	v_readfirstlane_b32 s16, v0
	s_addc_u32 s18, s7, s1
	s_lshl_b32 s0, s24, 2
	s_lshr_b32 s1, s16, 7
	s_add_i32 s14, s1, s0
	s_lshr_b32 s23, s16, 6
	s_lshl_b64 s[0:1], s[14:15], 13
	s_add_u32 s0, s2, s0
	v_and_b32_e32 v189, 31, v0
	s_addc_u32 s1, s3, s1
	s_lshl_b32 s21, s23, 5
	v_and_or_b32 v1, s21, 32, v189
	v_lshlrev_b32_e32 v186, 4, v1
	v_mov_b32_e32 v187, 0
	s_lshl_b32 s14, s23, 9
	v_lshl_add_u64 v[2:3], s[0:1], 0, v[186:187]
	s_and_b32 s0, s16, 0x3fffffc0
	s_lshl_b64 s[16:17], s[14:15], 1
	v_and_b32_e32 v188, 63, v0
	s_add_u32 s2, s11, s16
	s_addc_u32 s3, s12, s17
	s_add_u32 s44, s2, 0x8000
	s_addc_u32 s45, s3, 0
	v_lshlrev_b32_e32 v186, 4, v188
	v_lshl_add_u64 v[44:45], s[2:3], 0, v[186:187]
	s_add_u32 s2, s13, s16
	s_addc_u32 s3, s18, s17
	s_add_u32 s46, s2, 0x6000
	s_addc_u32 s47, s3, 0
	s_lshl_b32 s25, s23, 10
	s_cmp_lg_u32 0, -1
	s_cselect_b32 s1, 0, 0
	v_bfe_u32 v46, v0, 5, 1
	s_add_i32 s25, s25, s1
	s_mov_b32 s1, m0
	s_mov_b32 m0, s25
	s_nop 0
	global_load_lds_dwordx4 v[44:45], off
	s_mov_b32 m0, s1
	v_lshl_add_u64 v[34:35], s[2:3], 0, v[186:187]
	s_add_i32 s26, s25, 0x6000
	v_lshlrev_b32_e32 v4, 10, v46
	s_mov_b32 s1, m0
	s_mov_b32 m0, s26
	s_nop 0
	global_load_lds_dwordx4 v[34:35], off
	s_mov_b32 m0, s1
	s_mov_b64 s[18:19], 0x2000
	v_mov_b32_e32 v5, v187
	v_lshl_add_u64 v[6:7], v[44:45], 0, s[18:19]
	s_add_i32 s1, s25, 0x2000
	s_mov_b32 s2, m0
	s_mov_b32 m0, s1
	s_nop 0
	global_load_lds_dwordx4 v[6:7], off
	s_mov_b32 m0, s2
	v_lshl_add_u64 v[2:3], v[2:3], 0, v[4:5]
	global_load_dwordx4 v[136:139], v[2:3], off
	global_load_dwordx4 v[128:131], v[2:3], off offset:2048
	s_movk_i32 s1, 0x1000
	v_add_co_u32_e32 v2, vcc, s1, v2
	v_lshlrev_b32_e32 v1, 4, v189
	s_nop 0
	v_addc_co_u32_e32 v3, vcc, 0, v3, vcc
	global_load_dwordx4 v[120:123], v[2:3], off
	global_load_dwordx4 v[112:115], v[2:3], off offset:2048
	v_add3_u32 v184, 0, v4, v1
	v_mov_b32_e32 v2, v187
	v_mov_b32_e32 v3, v187
	v_mov_b32_e32 v4, v187
	v_mov_b32_e32 v6, v187
	v_mov_b32_e32 v7, v187
	v_mov_b32_e32 v8, v187
	v_mov_b32_e32 v9, v187
	v_mov_b32_e32 v10, v187
	v_mov_b32_e32 v11, v187
	v_mov_b32_e32 v12, v187
	v_mov_b32_e32 v13, v187
	v_mov_b32_e32 v14, v187
	v_mov_b32_e32 v15, v187
	v_mov_b32_e32 v16, v187
	v_mov_b32_e32 v17, v187
	s_mov_b64 s[2:3], 0x4000
	v_lshl_add_u64 v[18:19], v[44:45], 0, s[2:3]
	s_add_i32 s1, s25, 0x4000
	s_mov_b32 s11, m0
	s_mov_b32 m0, s1
	s_nop 0
	global_load_lds_dwordx4 v[18:19], off
	s_mov_b32 m0, s11
	v_lshl_add_u64 v[18:19], v[34:35], 0, s[18:19]
	s_add_i32 s1, s25, 0x8000
	s_mov_b32 s11, m0
	s_mov_b32 m0, s1
	s_nop 0
	global_load_lds_dwordx4 v[18:19], off
	s_mov_b32 m0, s11
	s_waitcnt vmcnt(4) lgkmcnt(0)
	s_barrier
	ds_read_b128 v[36:39], v184
	ds_read_b128 v[40:43], v184 offset:512
	v_lshlrev_b32_e32 v190, 3, v0
	s_mov_b64 s[12:13], 0x6000
	s_or_b32 s14, s22, s20
	s_sub_i32 s14, s14, s30
	s_add_i32 s34, s14, 16
	s_lshl_b32 s0, s0, 2
	s_ashr_i32 s35, s34, 31
	s_lshl_b64 s[34:35], s[34:35], 18
	s_mov_b32 s27, -1
	s_waitcnt vmcnt(3) lgkmcnt(1)
	v_mfma_f32_32x32x16_f16 v[18:33], v[36:39], v[136:139], v[2:17]
	s_movk_i32 s28, 0x6000
	s_movk_i32 s31, 0x2000
	s_movk_i32 s29, 0x4000
	v_lshlrev_b32_e32 v191, 9, v46
	v_lshlrev_b32_e32 v182, 4, v46
	v_lshlrev_b32_e32 v180, 4, v188
	s_waitcnt lgkmcnt(0)
	v_mfma_f32_32x32x16_f16 v[2:17], v[40:43], v[136:139], v[2:17]
	ds_read_b128 v[36:39], v184 offset:2048
	ds_read_b128 v[40:43], v184 offset:2560
	s_waitcnt vmcnt(2) lgkmcnt(1)
	v_mfma_f32_32x32x16_f16 v[18:33], v[36:39], v[128:131], v[18:33]
	s_waitcnt lgkmcnt(0)
	v_mfma_f32_32x32x16_f16 v[2:17], v[40:43], v[128:131], v[2:17]
	ds_read_b128 v[36:39], v184 offset:4096
	ds_read_b128 v[40:43], v184 offset:4608
	s_waitcnt vmcnt(1) lgkmcnt(1)
	v_mfma_f32_32x32x16_f16 v[18:33], v[36:39], v[120:123], v[18:33]
	s_waitcnt lgkmcnt(0)
	v_mfma_f32_32x32x16_f16 v[2:17], v[40:43], v[120:123], v[2:17]
	ds_read_b128 v[36:39], v184 offset:6144
	ds_read_b128 v[40:43], v184 offset:6656
	s_waitcnt vmcnt(0) lgkmcnt(1)
	v_mfma_f32_32x32x16_f16 v[18:33], v[36:39], v[112:115], v[18:33]
	s_waitcnt lgkmcnt(0)
	v_mfma_f32_32x32x16_f16 v[2:17], v[40:43], v[112:115], v[2:17]
	s_nop 11
	v_max_f32_e32 v1, v19, v18
	v_max3_f32 v37, v20, v21, v3
	v_max3_f32 v1, v1, v2, v4
	v_max3_f32 v36, v37, v24, v25
	v_max3_f32 v1, v1, v5, v22
	v_max3_f32 v36, v36, v8, v9
	v_max3_f32 v1, v1, v23, v6
	v_max3_f32 v36, v36, v28, v29
	v_max3_f32 v1, v1, v7, v26
	v_max3_f32 v36, v36, v12, v13
	v_max3_f32 v1, v1, v27, v10
	v_max3_f32 v36, v36, v32, v33
	v_max3_f32 v1, v1, v11, v30
	v_max3_f32 v36, v36, v16, v17
	v_max3_f32 v1, v1, v31, v14
	v_max3_f32 v1, v1, v15, v36
	v_mov_b32_e32 v36, v1
	s_nop 1
	v_permlane32_swap_b32_e32 v1, v36
	v_max_f32_e32 v183, v36, v1
	v_lshlrev_b32_e32 v1, 1, v0
	v_sub_f32_e32 v36, v2, v183
	v_and_b32_e32 v1, 32, v1
	v_and_b32_e32 v2, 24, v190
	v_lshlrev_b32_e32 v0, 4, v0
	v_add3_u32 v1, 0, v1, v2
	v_and_b32_e32 v0, 0xc0, v0
	v_lshlrev_b32_e32 v2, 8, v46
	v_add3_u32 v181, v1, v2, v0
	v_xor_b32_e32 v0, 0x80000000, v183
	v_sub_f32_e32 v37, v3, v183
	v_sub_f32_e32 v38, v4, v183
	v_sub_f32_e32 v39, v5, v183
	v_sub_f32_e32 v40, v6, v183
	v_sub_f32_e32 v41, v7, v183
	v_sub_f32_e32 v42, v8, v183
	v_sub_f32_e32 v43, v9, v183
	v_sub_f32_e32 v47, v10, v183
	v_sub_f32_e32 v57, v11, v183
	v_sub_f32_e32 v58, v12, v183
	v_sub_f32_e32 v59, v13, v183
	v_sub_f32_e32 v60, v14, v183
	v_sub_f32_e32 v61, v15, v183
	v_mov_b32_e32 v1, v0
	v_mov_b32_e32 v2, v0
	v_mov_b32_e32 v3, v0
	v_mov_b32_e32 v4, v0
	v_mov_b32_e32 v5, v0
	v_mov_b32_e32 v6, v0
	v_mov_b32_e32 v7, v0
	v_mov_b32_e32 v8, v0
	v_mov_b32_e32 v9, v0
	v_mov_b32_e32 v10, v0
	v_mov_b32_e32 v11, v0
	v_mov_b32_e32 v12, v0
	v_mov_b32_e32 v13, v0
	v_mov_b32_e32 v14, v0
	v_mov_b32_e32 v15, v0
	s_waitcnt vmcnt(0) lgkmcnt(0)
	s_barrier
	v_sub_f32_e32 v62, v16, v183
	v_sub_f32_e32 v63, v17, v183
	v_lshl_add_u64 v[16:17], v[44:45], 0, s[12:13]
	s_mov_b32 s1, m0
	s_mov_b32 m0, s25
	s_nop 0
	global_load_lds_dwordx4 v[16:17], off
	s_mov_b32 m0, s1
	s_add_i32 s1, s25, 0xa000
	v_lshl_add_u64 v[16:17], v[34:35], 0, s[2:3]
	s_mov_b32 s11, m0
	s_mov_b32 m0, s1
	s_nop 0
	global_load_lds_dwordx4 v[16:17], off
	s_mov_b32 m0, s11
	ds_read_b128 v[172:175], v184 offset:8192
	ds_read_b128 v[168:171], v184 offset:8704
	ds_read_b128 v[164:167], v184 offset:10240
	ds_read_b128 v[160:163], v184 offset:10752
	ds_read_b128 v[156:159], v184 offset:12288
	ds_read_b128 v[152:155], v184 offset:12800
	ds_read_b128 v[148:151], v184 offset:14336
	ds_read_b128 v[144:147], v184 offset:14848
	s_add_i32 s11, s0, 0
	v_sub_f32_e32 v18, v18, v183
	v_sub_f32_e32 v19, v19, v183
	v_sub_f32_e32 v20, v20, v183
	v_sub_f32_e32 v21, v21, v183
	v_sub_f32_e32 v22, v22, v183
	v_sub_f32_e32 v23, v23, v183
	v_sub_f32_e32 v24, v24, v183
	v_sub_f32_e32 v25, v25, v183
	v_sub_f32_e32 v26, v26, v183
	v_sub_f32_e32 v27, v27, v183
	v_sub_f32_e32 v28, v28, v183
	v_sub_f32_e32 v29, v29, v183
	v_sub_f32_e32 v30, v30, v183
	v_sub_f32_e32 v31, v31, v183
	v_sub_f32_e32 v32, v32, v183
	v_sub_f32_e32 v33, v33, v183
	s_add_u32 s14, s16, s34
	v_exp_f32_e32 v64, v18
	v_exp_f32_e32 v65, v19
	v_exp_f32_e32 v48, v36
	v_exp_f32_e32 v49, v37
	v_exp_f32_e32 v66, v20
	v_exp_f32_e32 v50, v38
	v_exp_f32_e32 v67, v21
	v_exp_f32_e32 v51, v39
	v_exp_f32_e32 v68, v22
	v_exp_f32_e32 v52, v40
	v_exp_f32_e32 v69, v23
	v_exp_f32_e32 v53, v41
	v_exp_f32_e32 v70, v24
	v_exp_f32_e32 v54, v42
	v_exp_f32_e32 v71, v25
	v_exp_f32_e32 v55, v43
	v_exp_f32_e32 v72, v26
	v_exp_f32_e32 v56, v47
	v_exp_f32_e32 v73, v27
	v_exp_f32_e32 v57, v57
	v_exp_f32_e32 v74, v28
	v_exp_f32_e32 v58, v58
	v_exp_f32_e32 v75, v29
	v_exp_f32_e32 v59, v59
	v_exp_f32_e32 v76, v30
	v_exp_f32_e32 v60, v60
	v_exp_f32_e32 v77, v31
	v_exp_f32_e32 v61, v61
	v_exp_f32_e32 v78, v32
	v_exp_f32_e32 v62, v62
	v_exp_f32_e32 v79, v33
	v_exp_f32_e32 v63, v63
	s_addc_u32 s16, s17, s35
	v_cmp_gt_u32_e64 s[0:1], 32, v188
	s_mov_b32 s16, 0x41000000
	s_mov_b32 s36, 0x43800000
	s_mov_b64 s[4:5], 0x8000
	s_movk_i32 s14, 0x2000
	s_movk_i32 s19, 0x4000
	v_mov_b32_e32 v16, v187
	v_mov_b32_e32 v17, v187
	v_mov_b32_e32 v18, v187
	v_mov_b32_e32 v19, v187
	v_mov_b32_e32 v20, v187
	v_mov_b32_e32 v21, v187
	v_mov_b32_e32 v22, v187
	v_mov_b32_e32 v23, v187
	v_mov_b32_e32 v24, v187
	v_mov_b32_e32 v25, v187
	v_mov_b32_e32 v26, v187
	v_mov_b32_e32 v27, v187
	v_mov_b32_e32 v28, v187
	v_mov_b32_e32 v29, v187
	v_mov_b32_e32 v30, v187
	v_mov_b32_e32 v31, v187
	v_mov_b32_e32 v32, v187
	v_mov_b32_e32 v33, v187
	v_mov_b32_e32 v34, v187
	v_mov_b32_e32 v35, v187
	v_mov_b32_e32 v36, v187
	v_mov_b32_e32 v37, v187
	v_mov_b32_e32 v38, v187
	v_mov_b32_e32 v39, v187
	v_mov_b32_e32 v40, v187
	v_mov_b32_e32 v41, v187
	v_mov_b32_e32 v42, v187
	v_mov_b32_e32 v43, v187
	v_mov_b32_e32 v44, v187
	v_mov_b32_e32 v45, v187
	v_mov_b32_e32 v46, v187
	v_mov_b32_e32 v47, v187
	v_lshl_add_u32 v186, v189, 2, s11
	s_waitcnt vmcnt(2) lgkmcnt(0)
	s_barrier

.Lmy_back_3:
	v_add_f32_e32 v176, v187, v48
.LBB2_16:
	s_waitcnt lgkmcnt(14)
	v_mfma_f32_32x32x16_f16 v[16:31], v[140:143], v[96:99], v[16:31]
	v_exp_f32_e32 v80, v80
	v_exp_f32_e32 v81, v81
	v_exp_f32_e32 v82, v82
	v_exp_f32_e32 v83, v83
	s_waitcnt lgkmcnt(12)
	v_mfma_f32_32x32x16_f16 v[32:47], v[140:143], v[64:67], v[32:47]
	v_exp_f32_e32 v84, v84
	v_exp_f32_e32 v85, v85
	v_exp_f32_e32 v86, v86
	v_exp_f32_e32 v87, v87
	s_waitcnt lgkmcnt(10)
	v_mfma_f32_32x32x16_f16 v[16:31], v[132:135], v[68:71], v[16:31]
	v_exp_f32_e32 v88, v88
	v_exp_f32_e32 v89, v89
	v_exp_f32_e32 v90, v90
	v_exp_f32_e32 v91, v91
	s_waitcnt lgkmcnt(8)
	v_mfma_f32_32x32x16_f16 v[32:47], v[132:135], v[72:75], v[32:47]
	v_exp_f32_e32 v92, v92
	v_exp_f32_e32 v93, v93
	v_exp_f32_e32 v94, v94
	v_exp_f32_e32 v95, v95
	s_waitcnt lgkmcnt(6)
	v_mfma_f32_32x32x16_f16 v[16:31], v[124:127], v[76:79], v[16:31]
	v_exp_f32_e32 v0, v0
	v_exp_f32_e32 v1, v1
	v_exp_f32_e32 v2, v2
	v_exp_f32_e32 v3, v3
	s_waitcnt lgkmcnt(4)
	v_mfma_f32_32x32x16_f16 v[32:47], v[124:127], v[100:103], v[32:47]
	v_exp_f32_e32 v4, v4
	v_exp_f32_e32 v5, v5
	v_exp_f32_e32 v6, v6
	v_exp_f32_e32 v7, v7
	s_waitcnt lgkmcnt(2)
	v_mfma_f32_32x32x16_f16 v[16:31], v[116:119], v[104:107], v[16:31]
	v_exp_f32_e32 v8, v8
	v_exp_f32_e32 v9, v9
	v_exp_f32_e32 v10, v10
	v_exp_f32_e32 v11, v11
	s_waitcnt lgkmcnt(0)
	v_mfma_f32_32x32x16_f16 v[32:47], v[116:119], v[108:111], v[32:47]
	v_exp_f32_e32 v12, v12
	v_exp_f32_e32 v13, v13
	v_exp_f32_e32 v14, v14
	v_exp_f32_e32 v15, v15
	v_add_u32_e32 v48, s11, v182
